# B3: all barrier waiters poll the cross-XCC arrival counter TOP (target (gen+1)*nx) directly; TOPGEN/XGEN release atomics dropped; on top of B1+E2c+E8b
# baseline (speedup 1.0000x reference)
.LBB0_165:
	s_or_b64 exec, exec, s[8:9]
	v_cvt_f32_u32_e32 v4, v2
	s_waitcnt vmcnt(0)
	v_readfirstlane_b32 s6, v3
	v_sub_u32_e32 v3, 0, v2
	v_rcp_iflag_f32_e32 v4, v4
	v_add_u32_e32 v5, s6, v1
	v_mul_f32_e32 v4, 0x4f7ffffe, v4
	v_cvt_u32_f32_e32 v4, v4
	v_mul_lo_u32 v1, v3, v4
	v_mul_hi_u32 v1, v4, v1
	v_add_u32_e32 v1, v4, v1
	v_mul_hi_u32 v1, v5, v1
	v_mul_lo_u32 v3, v1, v2
	v_sub_u32_e32 v3, v5, v3
	v_add_u32_e32 v4, 1, v1
	v_cmp_ge_u32_e32 vcc, v3, v2
	s_nop 1
	v_cndmask_b32_e32 v1, v1, v4, vcc
	v_sub_u32_e32 v4, v3, v2
	v_cndmask_b32_e32 v3, v3, v4, vcc
	v_add_u32_e32 v4, 1, v1
	v_cmp_ge_u32_e32 vcc, v3, v2
	v_add_u32_e32 v3, 1, v5
	s_nop 0
	v_cndmask_b32_e32 v1, v1, v4, vcc
	v_mul_lo_u32 v4, v2, v1
	v_add_u32_e32 v2, v4, v2
	v_cmp_ne_u32_e32 vcc, v3, v2
	s_and_saveexec_b64 s[6:7], vcc
	s_xor_b64 s[6:7], exec, s[6:7]
	s_cbranch_execz .LBB0_179
	s_waitcnt lgkmcnt(0)
	v_mad_u32_u24 v3, v1, v0, v0
	v_mov_b32_e32 v0, 0
	s_add_u32 s12, s2, 0x13400
	s_addc_u32 s13, s3, 0
	global_load_dword v0, v0, s[12:13] sc1
	s_waitcnt vmcnt(0)
	v_cmp_lt_u32_e32 vcc, v0, v3
	s_and_saveexec_b64 s[8:9], vcc
	s_cbranch_execz .LBB0_178
	s_add_u32 s10, s2, 0x10200
	s_addc_u32 s11, s3, 0
	s_mov_b32 s24, 1
	s_mov_b64 s[14:15], 0
	v_mov_b32_e32 v0, 0
	s_branch .LBB0_169

.LBB0_171:
	global_load_dword v2, v0, s[12:13] sc1
	s_add_i32 s24, s24, 1
	s_mov_b64 s[20:21], -1
	s_waitcnt vmcnt(0)
	v_cmp_ge_u32_e32 vcc, v2, v3
	s_orn2_b64 s[18:19], vcc, exec
	s_branch .LBB0_168

.LBB0_182:
	s_or_b64 exec, exec, s[8:9]
	v_cvt_f32_u32_e32 v3, v0
	s_waitcnt vmcnt(0)
	v_readfirstlane_b32 s6, v2
	s_add_u32 s8, s2, 0x13500
	s_addc_u32 s9, s3, 0
	v_rcp_iflag_f32_e32 v3, v3
	v_add_u32_e32 v1, s6, v1
	v_add_u32_e32 v4, 1, v1
	s_mov_b64 s[10:11], 0
	v_mul_f32_e32 v2, 0x4f7ffffe, v3
	v_cvt_u32_f32_e32 v2, v2
	v_sub_u32_e32 v3, 0, v0
	v_mul_lo_u32 v3, v3, v2
	v_mul_hi_u32 v3, v2, v3
	v_add_u32_e32 v2, v2, v3
	v_mul_hi_u32 v2, v1, v2
	v_mul_lo_u32 v3, v2, v0
	v_sub_u32_e32 v1, v1, v3
	v_add_u32_e32 v5, 1, v2
	v_cmp_ge_u32_e32 vcc, v1, v0
	v_sub_u32_e32 v3, v1, v0
	s_nop 0
	v_cndmask_b32_e32 v2, v2, v5, vcc
	v_cndmask_b32_e32 v1, v1, v3, vcc
	v_add_u32_e32 v3, 1, v2
	v_cmp_ge_u32_e32 vcc, v1, v0
	s_nop 1
	v_cndmask_b32_e32 v2, v2, v3, vcc
	v_mul_lo_u32 v1, v0, v2
	v_add_u32_e32 v0, v1, v0
	v_cmp_ne_u32_e32 vcc, v4, v0
	v_mov_b32_e32 v3, v0
	v_mov_b64_e32 v[0:1], s[8:9]
	s_and_saveexec_b64 s[6:7], vcc
	s_cbranch_execz .LBB0_194
	v_mov_b32_e32 v0, 0
	global_load_dword v1, v0, s[8:9] offset:-256 sc1
	s_mov_b64 s[14:15], 0
	s_waitcnt vmcnt(0)
	v_cmp_lt_u32_e32 vcc, v1, v3
	s_and_saveexec_b64 s[12:13], vcc
	s_cbranch_execz .LBB0_193
	s_add_u32 s10, s2, 0x10200
	s_addc_u32 s11, s3, 0
	s_mov_b32 s22, 1
	s_mov_b64 s[2:3], 0
	s_branch .LBB0_186

.LBB0_188:
	global_load_dword v1, v0, s[8:9] offset:-256 sc1
	s_add_i32 s22, s22, 1
	s_mov_b64 s[16:17], -1
	s_waitcnt vmcnt(0)
	v_cmp_ge_u32_e32 vcc, v1, v3
	s_orn2_b64 s[20:21], vcc, exec
	s_branch .LBB0_185

.LBB0_196:
	s_or_b64 exec, exec, s[2:3]
	s_mov_b64 s[2:3], exec
	v_mbcnt_lo_u32_b32 v0, s2, 0
	v_mbcnt_hi_u32_b32 v0, s3, v0
	v_cmp_eq_u32_e32 vcc, 0, v0
	s_waitcnt vmcnt(0)
	buffer_inv sc1
	s_and_saveexec_b64 s[6:7], vcc
	s_cbranch_execz .LBB0_198
	s_bcnt1_i32_b64 s2, s[2:3]
	v_mov_b32_e32 v0, 0x2000
	v_mov_b32_e32 v1, s2
.LBB0_198:
	s_or_b64 exec, exec, s[6:7]
	s_waitcnt vmcnt(0)

.LBB0_220:
	s_or_b64 exec, exec, s[8:9]
	v_cvt_f32_u32_e32 v4, v2
	s_waitcnt vmcnt(0)
	v_readfirstlane_b32 s6, v3
	v_sub_u32_e32 v3, 0, v2
	v_rcp_iflag_f32_e32 v4, v4
	v_add_u32_e32 v5, s6, v1
	v_mul_f32_e32 v4, 0x4f7ffffe, v4
	v_cvt_u32_f32_e32 v4, v4
	v_mul_lo_u32 v1, v3, v4
	v_mul_hi_u32 v1, v4, v1
	v_add_u32_e32 v1, v4, v1
	v_mul_hi_u32 v1, v5, v1
	v_mul_lo_u32 v3, v1, v2
	v_sub_u32_e32 v3, v5, v3
	v_add_u32_e32 v4, 1, v1
	v_cmp_ge_u32_e32 vcc, v3, v2
	s_nop 1
	v_cndmask_b32_e32 v1, v1, v4, vcc
	v_sub_u32_e32 v4, v3, v2
	v_cndmask_b32_e32 v3, v3, v4, vcc
	v_add_u32_e32 v4, 1, v1
	v_cmp_ge_u32_e32 vcc, v3, v2
	v_add_u32_e32 v3, 1, v5
	s_nop 0
	v_cndmask_b32_e32 v1, v1, v4, vcc
	v_mul_lo_u32 v4, v2, v1
	v_add_u32_e32 v2, v4, v2
	v_cmp_ne_u32_e32 vcc, v3, v2
	s_and_saveexec_b64 s[6:7], vcc
	s_xor_b64 s[6:7], exec, s[6:7]
	s_cbranch_execz .LBB0_234
	s_waitcnt lgkmcnt(0)
	v_mad_u32_u24 v3, v1, v0, v0
	v_mov_b32_e32 v0, 0
	s_add_u32 s12, s0, 0x13400
	s_addc_u32 s13, s1, 0
	global_load_dword v0, v0, s[12:13] sc1
	s_waitcnt vmcnt(0)
	v_cmp_lt_u32_e32 vcc, v0, v3
	s_and_saveexec_b64 s[8:9], vcc
	s_cbranch_execz .LBB0_233
	s_add_u32 s10, s0, 0x10200
	s_addc_u32 s11, s1, 0
	s_mov_b32 s24, 1
	s_mov_b64 s[14:15], 0
	v_mov_b32_e32 v0, 0
	s_branch .LBB0_224

.LBB0_237:
	s_or_b64 exec, exec, s[8:9]
	v_cvt_f32_u32_e32 v3, v0
	s_waitcnt vmcnt(0)
	v_readfirstlane_b32 s6, v2
	s_add_u32 s8, s0, 0x13500
	s_addc_u32 s9, s1, 0
	v_rcp_iflag_f32_e32 v3, v3
	v_add_u32_e32 v1, s6, v1
	v_add_u32_e32 v4, 1, v1
	s_mov_b64 s[10:11], 0
	v_mul_f32_e32 v2, 0x4f7ffffe, v3
	v_cvt_u32_f32_e32 v2, v2
	v_sub_u32_e32 v3, 0, v0
	v_mul_lo_u32 v3, v3, v2
	v_mul_hi_u32 v3, v2, v3
	v_add_u32_e32 v2, v2, v3
	v_mul_hi_u32 v2, v1, v2
	v_mul_lo_u32 v3, v2, v0
	v_sub_u32_e32 v1, v1, v3
	v_add_u32_e32 v5, 1, v2
	v_cmp_ge_u32_e32 vcc, v1, v0
	v_sub_u32_e32 v3, v1, v0
	s_nop 0
	v_cndmask_b32_e32 v2, v2, v5, vcc
	v_cndmask_b32_e32 v1, v1, v3, vcc
	v_add_u32_e32 v3, 1, v2
	v_cmp_ge_u32_e32 vcc, v1, v0
	s_nop 1
	v_cndmask_b32_e32 v2, v2, v3, vcc
	v_mul_lo_u32 v1, v0, v2
	v_add_u32_e32 v0, v1, v0
	v_cmp_ne_u32_e32 vcc, v4, v0
	v_mov_b32_e32 v3, v0
	v_mov_b64_e32 v[0:1], s[8:9]
	s_and_saveexec_b64 s[6:7], vcc
	s_cbranch_execz .LBB0_249
	v_mov_b32_e32 v0, 0
	global_load_dword v1, v0, s[8:9] offset:-256 sc1
	s_mov_b64 s[14:15], 0
	s_waitcnt vmcnt(0)
	v_cmp_lt_u32_e32 vcc, v1, v3
	s_and_saveexec_b64 s[12:13], vcc
	s_cbranch_execz .LBB0_248
	s_add_u32 s10, s0, 0x10200
	s_addc_u32 s11, s1, 0
	s_mov_b32 s22, 1
	s_mov_b64 s[0:1], 0
	s_branch .LBB0_241

.LBB0_251:
	s_or_b64 exec, exec, s[0:1]
	s_mov_b64 s[0:1], exec
	v_mbcnt_lo_u32_b32 v0, s0, 0
	v_mbcnt_hi_u32_b32 v0, s1, v0
	v_cmp_eq_u32_e32 vcc, 0, v0
	s_waitcnt vmcnt(0)
	buffer_inv sc1
	s_and_saveexec_b64 s[6:7], vcc
	s_cbranch_execz .LBB0_253
	s_bcnt1_i32_b64 s0, s[0:1]
	v_mov_b32_e32 v0, 0x2000
	v_mov_b32_e32 v1, s0
.LBB0_253:
	s_or_b64 exec, exec, s[6:7]
	s_waitcnt vmcnt(0)

.LBB0_292:
	s_or_b64 exec, exec, s[8:9]
	v_cvt_f32_u32_e32 v4, v2
	s_waitcnt vmcnt(0)
	v_readfirstlane_b32 s6, v3
	v_sub_u32_e32 v3, 0, v2
	v_rcp_iflag_f32_e32 v4, v4
	v_add_u32_e32 v5, s6, v1
	v_mul_f32_e32 v4, 0x4f7ffffe, v4
	v_cvt_u32_f32_e32 v4, v4
	v_mul_lo_u32 v1, v3, v4
	v_mul_hi_u32 v1, v4, v1
	v_add_u32_e32 v1, v4, v1
	v_mul_hi_u32 v1, v5, v1
	v_mul_lo_u32 v3, v1, v2
	v_sub_u32_e32 v3, v5, v3
	v_add_u32_e32 v4, 1, v1
	v_cmp_ge_u32_e32 vcc, v3, v2
	s_nop 1
	v_cndmask_b32_e32 v1, v1, v4, vcc
	v_sub_u32_e32 v4, v3, v2
	v_cndmask_b32_e32 v3, v3, v4, vcc
	v_add_u32_e32 v4, 1, v1
	v_cmp_ge_u32_e32 vcc, v3, v2
	v_add_u32_e32 v3, 1, v5
	s_nop 0
	v_cndmask_b32_e32 v1, v1, v4, vcc
	v_mul_lo_u32 v4, v2, v1
	v_add_u32_e32 v2, v4, v2
	v_cmp_ne_u32_e32 vcc, v3, v2
	s_and_saveexec_b64 s[6:7], vcc
	s_xor_b64 s[6:7], exec, s[6:7]
	s_cbranch_execz .LBB0_306
	s_waitcnt lgkmcnt(0)
	v_mad_u32_u24 v2, v1, v0, v0
	s_add_u32 s12, s2, 0x13400
	s_addc_u32 s13, s3, 0
	global_load_dword v0, v169, s[12:13] sc1
	s_waitcnt vmcnt(0)
	v_cmp_lt_u32_e32 vcc, v0, v2
	s_and_saveexec_b64 s[8:9], vcc
	s_cbranch_execz .LBB0_305
	s_add_u32 s10, s2, 0x10200
	s_addc_u32 s11, s3, 0
	s_mov_b32 s24, 1
	s_mov_b64 s[14:15], 0
	s_branch .LBB0_296

.LBB0_298:
	global_load_dword v0, v169, s[12:13] sc1
	s_add_i32 s24, s24, 1
	s_mov_b64 s[20:21], -1
	s_waitcnt vmcnt(0)
	v_cmp_ge_u32_e32 vcc, v0, v2
	s_orn2_b64 s[18:19], vcc, exec
	s_branch .LBB0_295

.LBB0_309:
	s_or_b64 exec, exec, s[8:9]
	s_waitcnt vmcnt(0)
	v_readfirstlane_b32 s6, v2
	v_cvt_f32_u32_e32 v2, v0
	v_sub_u32_e32 v3, 0, v0
	v_add_u32_e32 v1, s6, v1
	s_add_u32 s6, s2, 0x13500
	v_rcp_iflag_f32_e32 v2, v2
	s_addc_u32 s7, s3, 0
	s_mov_b64 s[10:11], 0
	v_mul_f32_e32 v2, 0x4f7ffffe, v2
	v_cvt_u32_f32_e32 v2, v2
	v_mul_lo_u32 v3, v3, v2
	v_mul_hi_u32 v3, v2, v3
	v_add_u32_e32 v2, v2, v3
	v_mul_hi_u32 v2, v1, v2
	v_mul_lo_u32 v3, v2, v0
	v_sub_u32_e32 v3, v1, v3
	v_cmp_ge_u32_e32 vcc, v3, v0
	v_add_u32_e32 v4, 1, v2
	v_add_u32_e32 v1, 1, v1
	v_cndmask_b32_e32 v2, v2, v4, vcc
	v_sub_u32_e32 v4, v3, v0
	v_cndmask_b32_e32 v3, v3, v4, vcc
	v_cmp_ge_u32_e32 vcc, v3, v0
	v_add_u32_e32 v3, 1, v2
	s_nop 0
	v_cndmask_b32_e32 v2, v2, v3, vcc
	v_mul_lo_u32 v3, v0, v2
	v_add_u32_e32 v0, v3, v0
	v_cmp_ne_u32_e32 vcc, v1, v0
	v_mov_b32_e32 v3, v0
	v_mov_b64_e32 v[0:1], s[6:7]
	s_and_saveexec_b64 s[8:9], vcc
	s_cbranch_execz .LBB0_321
	global_load_dword v0, v169, s[6:7] offset:-256 sc1
	s_mov_b64 s[14:15], 0
	s_waitcnt vmcnt(0)
	v_cmp_lt_u32_e32 vcc, v0, v3
	s_and_saveexec_b64 s[12:13], vcc
	s_cbranch_execz .LBB0_320
	s_add_u32 s10, s2, 0x10200
	s_addc_u32 s11, s3, 0
	s_mov_b32 s22, 1
	s_mov_b64 s[2:3], 0
	s_branch .LBB0_313

.LBB0_315:
	global_load_dword v0, v169, s[6:7] offset:-256 sc1
	s_add_i32 s22, s22, 1
	s_mov_b64 s[18:19], -1
	s_waitcnt vmcnt(0)
	v_cmp_ge_u32_e32 vcc, v0, v3
	s_orn2_b64 s[16:17], vcc, exec
	s_branch .LBB0_312

.LBB0_323:
	s_or_b64 exec, exec, s[2:3]
	s_mov_b64 s[2:3], exec
	v_mbcnt_lo_u32_b32 v0, s2, 0
	v_mbcnt_hi_u32_b32 v0, s3, v0
	v_cmp_eq_u32_e32 vcc, 0, v0
	s_waitcnt vmcnt(0)
	buffer_inv sc1
	s_and_saveexec_b64 s[6:7], vcc
	s_cbranch_execz .LBB0_325
	s_bcnt1_i32_b64 s2, s[2:3]
	v_mov_b32_e32 v0, s2
.LBB0_325:
	s_or_b64 exec, exec, s[6:7]
	s_waitcnt vmcnt(0)

.LBB0_412:
	s_or_b64 exec, exec, s[2:3]
	s_mov_b64 s[2:3], exec
	v_mbcnt_lo_u32_b32 v0, s2, 0
	v_mbcnt_hi_u32_b32 v0, s3, v0
	v_cmp_eq_u32_e32 vcc, 0, v0
	s_waitcnt vmcnt(0)
	buffer_inv sc1
	s_and_saveexec_b64 s[6:7], vcc
	s_cbranch_execz .LBB0_414
	s_bcnt1_i32_b64 s2, s[2:3]
	v_mov_b32_e32 v0, s2
.LBB0_414:
	s_or_b64 exec, exec, s[6:7]
	s_waitcnt vmcnt(0)

.LBB0_516:
	s_or_b64 exec, exec, s[2:3]
	s_mov_b64 s[2:3], exec
	v_mbcnt_lo_u32_b32 v0, s2, 0
	v_mbcnt_hi_u32_b32 v0, s3, v0
	v_cmp_eq_u32_e32 vcc, 0, v0
	s_waitcnt vmcnt(0)
	buffer_inv sc1
	s_and_saveexec_b64 s[6:7], vcc
	s_cbranch_execz .LBB0_518
	s_bcnt1_i32_b64 s2, s[2:3]
	v_mov_b32_e32 v0, s2
.LBB0_518:
	s_or_b64 exec, exec, s[6:7]
	s_waitcnt vmcnt(0)

.LBB0_669:
	s_or_b64 exec, exec, s[2:3]
	s_mov_b64 s[2:3], exec
	v_mbcnt_lo_u32_b32 v0, s2, 0
	v_mbcnt_hi_u32_b32 v0, s3, v0
	v_cmp_eq_u32_e32 vcc, 0, v0
	s_waitcnt vmcnt(0)
	buffer_inv sc1
	s_and_saveexec_b64 s[6:7], vcc
	s_cbranch_execz .LBB0_671
	s_bcnt1_i32_b64 s2, s[2:3]
	v_mov_b32_e32 v0, s2
.LBB0_671:
	s_or_b64 exec, exec, s[6:7]
	s_waitcnt vmcnt(0)

.LBB0_820:
	s_or_b64 exec, exec, s[2:3]
	s_mov_b64 s[2:3], exec
	v_mbcnt_lo_u32_b32 v0, s2, 0
	v_mbcnt_hi_u32_b32 v0, s3, v0
	v_cmp_eq_u32_e32 vcc, 0, v0
	s_waitcnt vmcnt(0)
	buffer_inv sc1
	s_and_saveexec_b64 s[6:7], vcc
	s_cbranch_execz .LBB0_822
	s_bcnt1_i32_b64 s2, s[2:3]
	v_mov_b32_e32 v0, s2
.LBB0_822:
	s_or_b64 exec, exec, s[6:7]
	s_waitcnt vmcnt(0)

.LBB0_980:
	s_or_b64 exec, exec, s[2:3]
	s_mov_b64 s[2:3], exec
	v_mbcnt_lo_u32_b32 v0, s2, 0
	v_mbcnt_hi_u32_b32 v0, s3, v0
	v_cmp_eq_u32_e32 vcc, 0, v0
	s_waitcnt vmcnt(0)
	buffer_inv sc1
	s_and_saveexec_b64 s[6:7], vcc
	s_cbranch_execz .LBB0_982
	s_bcnt1_i32_b64 s2, s[2:3]
	v_mov_b32_e32 v0, s2
.LBB0_982:
	s_or_b64 exec, exec, s[6:7]
	s_waitcnt vmcnt(0)

.LBB0_1122:
	s_or_b64 exec, exec, s[2:3]
	s_mov_b64 s[2:3], exec
	v_mbcnt_lo_u32_b32 v0, s2, 0
	v_mbcnt_hi_u32_b32 v0, s3, v0
	v_cmp_eq_u32_e32 vcc, 0, v0
	s_waitcnt vmcnt(0)
	buffer_inv sc1
	s_and_saveexec_b64 s[6:7], vcc
	s_cbranch_execz .LBB0_1124
	s_bcnt1_i32_b64 s2, s[2:3]
	v_mov_b32_e32 v0, s2
.LBB0_1124:
	s_or_b64 exec, exec, s[6:7]
	s_waitcnt vmcnt(0)

.LBB0_1179:
	s_or_b64 exec, exec, s[2:3]
	s_mov_b64 s[2:3], exec
	v_mbcnt_lo_u32_b32 v0, s2, 0
	v_mbcnt_hi_u32_b32 v0, s3, v0
	v_cmp_eq_u32_e32 vcc, 0, v0
	s_waitcnt vmcnt(0)
	buffer_inv sc1
	s_and_saveexec_b64 s[6:7], vcc
	s_cbranch_execz .LBB0_1181
	s_bcnt1_i32_b64 s2, s[2:3]
	v_mov_b32_e32 v0, s2
.LBB0_1181:
	s_or_b64 exec, exec, s[6:7]
	s_waitcnt vmcnt(0)

.LBB0_1247:
	s_or_b64 exec, exec, s[2:3]
	s_mov_b64 s[2:3], exec
	v_mbcnt_lo_u32_b32 v0, s2, 0
	v_mbcnt_hi_u32_b32 v0, s3, v0
	v_cmp_eq_u32_e32 vcc, 0, v0
	s_waitcnt vmcnt(0)
	buffer_inv sc1
	s_and_saveexec_b64 s[6:7], vcc
	s_cbranch_execz .LBB0_1249
	s_bcnt1_i32_b64 s2, s[2:3]
	v_mov_b32_e32 v0, s2
.LBB0_1249:
	s_or_b64 exec, exec, s[6:7]
	s_waitcnt vmcnt(0)

.LBB0_1347:
	s_or_b64 exec, exec, s[2:3]
	s_mov_b64 s[2:3], exec
	v_mbcnt_lo_u32_b32 v0, s2, 0
	v_mbcnt_hi_u32_b32 v0, s3, v0
	v_cmp_eq_u32_e32 vcc, 0, v0
	s_waitcnt vmcnt(0)
	buffer_inv sc1
	s_and_saveexec_b64 s[6:7], vcc
	s_cbranch_execz .LBB0_1349
	s_bcnt1_i32_b64 s2, s[2:3]
	v_mov_b32_e32 v0, s2
.LBB0_1349:
	s_or_b64 exec, exec, s[6:7]
	s_waitcnt vmcnt(0)

.LBB0_1480:
	s_or_b64 exec, exec, s[2:3]
	s_mov_b64 s[2:3], exec
	v_mbcnt_lo_u32_b32 v0, s2, 0
	v_mbcnt_hi_u32_b32 v0, s3, v0
	v_cmp_eq_u32_e32 vcc, 0, v0
	s_waitcnt vmcnt(0)
	buffer_inv sc1
	s_and_saveexec_b64 s[6:7], vcc
	s_cbranch_execz .LBB0_1482
	s_bcnt1_i32_b64 s2, s[2:3]
	v_mov_b32_e32 v0, s2
.LBB0_1482:
	s_or_b64 exec, exec, s[6:7]
	s_waitcnt vmcnt(0)

.LBB0_1577:
	s_or_b64 exec, exec, s[2:3]
	s_mov_b64 s[2:3], exec
	v_mbcnt_lo_u32_b32 v0, s2, 0
	v_mbcnt_hi_u32_b32 v0, s3, v0
	v_cmp_eq_u32_e32 vcc, 0, v0
	s_waitcnt vmcnt(0)
	buffer_inv sc1
	s_and_saveexec_b64 s[6:7], vcc
	s_cbranch_execz .LBB0_1579
	s_bcnt1_i32_b64 s2, s[2:3]
	v_mov_b32_e32 v0, s2
.LBB0_1579:
	s_or_b64 exec, exec, s[6:7]
	s_waitcnt vmcnt(0)

.LBB0_1661:
	s_bcnt1_i32_b64 s2, s[2:3]
	v_mov_b32_e32 v0, s2
	s_getpc_b64 s[98:99]
